# attention: static s_setprio 1 for waves 4-7 across the tile loop (on top of load-address folding)
# speedup vs baseline: 1.0000x; 1.0000x over previous
; __device__ __forceinline__ float swap_max(float v) { float r0, r1; swap32(v, r0, r1); return fmaxf(r0, r1); }
; #define AT_TRR(dst, off) asm volatile("ds_read_b64_tr_b16 %0, %1 offset:%c2" : "=&v"(dst) : "v"(vaddr), "i"(off) : "memory")
; #define AT_PIN() do { _Pragma("unroll") for (int g_ = 0; g_ < 4; ++g_) { __builtin_amdgcn_sched_group_barrier(0x008, 1, 0); __builtin_amdgcn_sched_group_barrier(0x400, 2, 0); __builtin_amdgcn_sched_group_barrier(0x002, 2, 0); } \
;                 __builtin_amdgcn_sched_barrier(0); } while (0)
; __device__ __forceinline__ void attn_unit(const Frame& F, const bf16* __restrict__ proj, bf16* mix, const float* relb, const float* subg, int h, int qb, float lam, float one_m_li) {
;     ...
;             float mx = fmaxf(fmaxf(p0[0], p0[1]), p1[0]), mb = fmaxf(fmaxf(p0[2], p0[3]), p1[1]); mx = fmaxf(fmaxf(mx, p1[2]), p1[3]);
; #pragma unroll
;             for (int r = 4; r < 16; r += 4) { mx = fmaxf(fmaxf(mx, p0[r]), p0[r + 1]); mb = fmaxf(fmaxf(mb, p0[r + 2]), p0[r + 3]); mx = fmaxf(fmaxf(mx, p1[r]), p1[r + 1]); mb = fmaxf(fmaxf(mb, p1[r + 2]), p1[r + 3]); }
;             mx = swap_max(fmaxf(mx, mb));
;             if (j == 0 || __any(mx > 8.0f)) {
;                 const float dl = (j == 0) ? mx : fmaxf(mx, 0.f); mrun += dl;
;                 const float alpha = __builtin_amdgcn_exp2f(-dl); lsum *= alpha;
; #pragma unroll
;                 for (int r = 0; r < 16; ++r) { p0[r] -= dl; p1[r] -= dl; negm[r] = -mrun; }
; #pragma unroll
;                 for (int eb = 0; eb < 4; ++eb)
; #pragma unroll
;                     for (int r = 0; r < 16; ++r) o[eb][r] *= alpha;
;             }
;             bf16x8 pb[4]; float lpart[4];
;     ...
;             AT_EXPBLK(0);
;             const unsigned vaddr = (unsigned)(uintptr_t)(lds + cur * STAGE + 16384 + (4 * hi + ((lane & 15) >> 2)) * 64 + ((lane >> 4) & 1) * 32 + (lane & 3) * 8);
;             s16x4 fl[2][4], fh[2][4];
;     ...
; #pragma unroll
;             for (int eb = 0; eb < 4; ++eb) { AT_TRR(fl[0][eb], eb * 4096); AT_TRR(fh[0][eb], eb * 4096 + 512); }
;     ...
;             AT_PVSTEP(0); AT_EXPBLK(1); AT_PIN();
;             AT_PVSTEP(1); AT_EXPBLK(2); AT_PIN();
;             AT_PVSTEP(2); AT_EXPBLK(3); AT_PIN();
;             AT_PVSTEP(3); __builtin_amdgcn_sched_barrier(0);
.LBB0_578:
	v_and_b32_e32 v213, 63, v32
	v_lshlrev_b32_e32 v34, 3, v32
	v_lshlrev_b32_e32 v32, 1, v32
	v_and_b32_e32 v219, 0xc0, v33
	v_and_b32_e32 v220, 32, v32
	s_nop 2
	v_max_f32_e32 v32, v1, v1
	v_max_f32_e32 v33, v0, v0
	v_max_f32_e32 v32, v33, v32
	v_max3_f32 v33, v2, v3, v17
	v_max3_f32 v32, v32, v16, v18
	v_max3_f32 v32, v32, v19, v4
	v_max3_f32 v33, v33, v6, v7
	v_max3_f32 v32, v32, v5, v20
	v_max3_f32 v33, v33, v22, v23
	v_max3_f32 v32, v32, v21, v8
	v_max3_f32 v33, v33, v10, v11
	v_max3_f32 v32, v32, v9, v24
	v_max3_f32 v33, v33, v26, v27
	v_max3_f32 v32, v32, v25, v12
	v_max3_f32 v33, v33, v14, v15
	v_max3_f32 v32, v32, v13, v28
	v_max3_f32 v33, v33, v30, v31
	v_max3_f32 v32, v32, v29, v33
	v_mov_b32_e32 v33, v32
	s_nop 1
	v_permlane32_swap_b32 v32, v33
	v_lshlrev_b32_e32 v218, 8, v187
	v_max_f32_e32 v33, v33, v33
	v_max_f32_e32 v32, v32, v32
	v_max_f32_e32 v82, v32, v33
	v_sub_f32_e32 v0, v0, v82
	v_exp_f32_e32 v84, v0
	v_add_u32_e32 v0, 0, v218
	v_and_b32_e32 v221, 24, v34
	v_sub_f32_e32 v1, v1, v82
	v_add3_u32 v0, v0, v219, v220
	v_sub_f32_e32 v2, v2, v82
	v_sub_f32_e32 v3, v3, v82
	v_sub_f32_e32 v85, v8, v82
	v_exp_f32_e64 v8, -v82
	v_exp_f32_e32 v86, v1
	v_add3_u32 v227, v0, v221, s17
	ds_read_b64_tr_b16 v[0:1], v227 offset:0
	v_sub_f32_e32 v4, v4, v82
	v_sub_f32_e32 v5, v5, v82
	v_exp_f32_e32 v96, v2
	v_exp_f32_e32 v98, v3
	ds_read_b64_tr_b16 v[2:3], v227 offset:512
	v_sub_f32_e32 v6, v6, v82
	v_sub_f32_e32 v7, v7, v82
	v_exp_f32_e32 v92, v4
	v_exp_f32_e32 v94, v5
	ds_read_b64_tr_b16 v[4:5], v227 offset:4096
	v_exp_f32_e32 v88, v6
	v_exp_f32_e32 v90, v7
	ds_read_b64_tr_b16 v[6:7], v227 offset:4608
	v_sub_f32_e32 v97, v9, v82
	v_mul_f32_e32 v64, 0, v8
	ds_read_b64_tr_b16 v[8:9], v227 offset:8192
	v_sub_f32_e32 v99, v10, v82
	v_sub_f32_e32 v100, v11, v82
	ds_read_b64_tr_b16 v[10:11], v227 offset:8704
	ds_read_b64_tr_b16 v[108:109], v227 offset:12288
	ds_read_b64_tr_b16 v[110:111], v227 offset:12800
	ds_read_b64_tr_b16 v[162:163], v227 offset:1024
	ds_read_b64_tr_b16 v[164:165], v227 offset:1536
	ds_read_b64_tr_b16 v[166:167], v227 offset:5120
	ds_read_b64_tr_b16 v[168:169], v227 offset:5632
	ds_read_b64_tr_b16 v[170:171], v227 offset:9216
	ds_read_b64_tr_b16 v[172:173], v227 offset:9728
	ds_read_b64_tr_b16 v[174:175], v227 offset:13312
	ds_read_b64_tr_b16 v[176:177], v227 offset:13824
	s_waitcnt lgkmcnt(8)
	s_lshr_b32 s10, s9, 6
	s_lshl_b32 s12, s8, 1
	s_add_i32 s11, s10, -2
	s_mov_b32 s13, 2
	s_add_i32 s14, s12, 2
	v_mov_b32_e32 v65, v64
	v_mov_b32_e32 v66, v64
	v_mov_b32_e32 v67, v64
	v_mov_b32_e32 v68, v64
	v_mov_b32_e32 v69, v64
	v_mov_b32_e32 v70, v64
	v_mov_b32_e32 v71, v64
	v_mov_b32_e32 v72, v64
	v_mov_b32_e32 v73, v64
	v_mov_b32_e32 v74, v64
	v_mov_b32_e32 v75, v64
	v_mov_b32_e32 v76, v64
	v_mov_b32_e32 v77, v64
	v_mov_b32_e32 v78, v64
	v_mov_b32_e32 v79, v64
	v_sub_f32_e32 v83, v16, v82
	v_sub_f32_e32 v87, v17, v82
	v_sub_f32_e32 v89, v18, v82
	v_sub_f32_e32 v91, v19, v82
	v_sub_f32_e32 v93, v20, v82
	v_sub_f32_e32 v95, v21, v82
	v_sub_f32_e32 v101, v22, v82
	v_sub_f32_e32 v196, v23, v82
	v_sub_f32_e32 v197, v24, v82
	v_sub_f32_e32 v198, v25, v82
	v_sub_f32_e32 v199, v26, v82
	v_sub_f32_e32 v200, v27, v82
	v_sub_f32_e32 v201, v28, v82
	v_sub_f32_e32 v202, v29, v82
	v_sub_f32_e32 v203, v30, v82
	v_sub_f32_e32 v226, v31, v82
	v_sub_f32_e32 v178, v12, v82
	v_sub_f32_e32 v179, v13, v82
	v_sub_f32_e32 v180, v14, v82
	v_sub_f32_e32 v181, v15, v82
	v_cvt_pk_bf16_f32 v104, v84, v86
	v_cvt_pk_bf16_f32 v105, v96, v98
	v_cvt_pk_bf16_f32 v106, v92, v94
	v_cvt_pk_bf16_f32 v107, v88, v90
	s_nop 1
	v_mfma_f32_32x32x16_bf16 v[48:63], v[0:3], v[104:107], v[64:79]
	v_exp_f32_e32 v100, v100
	v_mfma_f32_32x32x16_bf16 v[32:47], v[4:7], v[104:107], v[64:79]
	v_mfma_f32_32x32x16_bf16 v[16:31], v[8:11], v[104:107], v[64:79]
	v_mov_b64_e32 v[0:1], v[64:65]
	v_mov_b64_e32 v[12:13], v[76:77]
	v_mov_b64_e32 v[14:15], v[78:79]
	v_mov_b64_e32 v[8:9], v[72:73]
	v_mov_b64_e32 v[10:11], v[74:75]
	v_mov_b64_e32 v[2:3], v[66:67]
	v_mov_b64_e32 v[4:5], v[68:69]
	v_mov_b64_e32 v[6:7], v[70:71]
	v_exp_f32_e32 v72, v181
	v_exp_f32_e32 v76, v179
	v_exp_f32_e32 v70, v180
	v_exp_f32_e32 v78, v99
	v_exp_f32_e32 v74, v178
	v_mfma_f32_32x32x16_bf16 v[0:15], v[108:111], v[104:107], v[0:15]
	v_exp_f32_e32 v66, v85
	v_exp_f32_e32 v68, v97
	v_cvt_pk_bf16_f32 v105, v78, v100
	v_cvt_pk_bf16_f32 v106, v74, v76
	v_cvt_pk_bf16_f32 v107, v70, v72
	v_cvt_pk_bf16_f32 v104, v66, v68
	ds_read_b64_tr_b16 v[108:109], v227 offset:2048
	ds_read_b64_tr_b16 v[110:111], v227 offset:2560
	ds_read_b64_tr_b16 v[178:179], v227 offset:6144
	ds_read_b64_tr_b16 v[180:181], v227 offset:6656
	ds_read_b64_tr_b16 v[182:183], v227 offset:10240
	ds_read_b64_tr_b16 v[184:185], v227 offset:10752
	ds_read_b64_tr_b16 v[222:223], v227 offset:14336
	ds_read_b64_tr_b16 v[224:225], v227 offset:14848
	s_waitcnt lgkmcnt(8)
; #define AT_PIN() do { _Pragma("unroll") for (int g_ = 0; g_ < 4; ++g_) { __builtin_amdgcn_sched_group_barrier(0x008, 1, 0); __builtin_amdgcn_sched_group_barrier(0x400, 2, 0); __builtin_amdgcn_sched_group_barrier(0x002, 2, 0); } \
;                 __builtin_amdgcn_sched_barrier(0); } while (0)
; __device__ __forceinline__ void attn_unit(const Frame& F, const bf16* __restrict__ proj, bf16* mix, const float* relb, const float* subg, int h, int qb, float lam, float one_m_li) {
;     ...
;     const bf16* kbase = proj + C_K + h * 128; const bf16* vbase = proj + C_V + h * 128;
;     ...
;             AT_PVSTEP(0); AT_EXPBLK(1); AT_PIN();
;             AT_PVSTEP(1); AT_EXPBLK(2); AT_PIN();
;             AT_PVSTEP(2); AT_EXPBLK(3); AT_PIN();
;             AT_PVSTEP(3); __builtin_amdgcn_sched_barrier(0);
;             lsum += (lpart[0] + lpart[1]) + (lpart[2] + lpart[3]);
	s_nop 1
	v_mfma_f32_32x32x16_bf16 v[48:63], v[162:165], v[104:107], v[48:63]
	v_exp_f32_e32 v85, v83
	v_exp_f32_e32 v87, v87
	s_nop 0
	v_cvt_pk_bf16_f32 v162, v85, v87
	v_mfma_f32_32x32x16_bf16 v[32:47], v[166:169], v[104:107], v[32:47]
	v_exp_f32_e32 v97, v89
	v_exp_f32_e32 v99, v91
	s_nop 0
	v_cvt_pk_bf16_f32 v163, v97, v99
	v_mfma_f32_32x32x16_bf16 v[16:31], v[170:173], v[104:107], v[16:31]
	v_exp_f32_e32 v93, v93
	v_exp_f32_e32 v95, v95
	s_nop 0
	v_cvt_pk_bf16_f32 v164, v93, v95
	v_mfma_f32_32x32x16_bf16 v[0:15], v[174:177], v[104:107], v[0:15]
	v_exp_f32_e32 v89, v101
	v_exp_f32_e32 v91, v196
	s_nop 0
	v_cvt_pk_bf16_f32 v165, v89, v91
	ds_read_b64_tr_b16 v[104:105], v227 offset:3072
	ds_read_b64_tr_b16 v[106:107], v227 offset:3584
	ds_read_b64_tr_b16 v[166:167], v227 offset:7168
	ds_read_b64_tr_b16 v[168:169], v227 offset:7680
	ds_read_b64_tr_b16 v[170:171], v227 offset:11264
	ds_read_b64_tr_b16 v[172:173], v227 offset:11776
	ds_read_b64_tr_b16 v[174:175], v227 offset:15360
	ds_read_b64_tr_b16 v[176:177], v227 offset:15872
	s_waitcnt lgkmcnt(8)
	s_nop 1
	v_mfma_f32_32x32x16_bf16 v[48:63], v[108:111], v[162:165], v[48:63]
	v_exp_f32_e32 v67, v197
	v_exp_f32_e32 v69, v198
	s_nop 0
	v_cvt_pk_bf16_f32 v108, v67, v69
	v_mfma_f32_32x32x16_bf16 v[32:47], v[178:181], v[162:165], v[32:47]
	v_exp_f32_e32 v79, v199
	v_exp_f32_e32 v101, v200
	s_nop 0
	v_cvt_pk_bf16_f32 v109, v79, v101
	v_mfma_f32_32x32x16_bf16 v[16:31], v[182:185], v[162:165], v[16:31]
	v_exp_f32_e32 v75, v201
	v_exp_f32_e32 v77, v202
	s_nop 0
	v_cvt_pk_bf16_f32 v110, v75, v77
	v_mfma_f32_32x32x16_bf16 v[0:15], v[222:225], v[162:165], v[0:15]
	v_exp_f32_e32 v71, v203
	v_exp_f32_e32 v73, v226
	s_nop 0
	v_cvt_pk_bf16_f32 v111, v71, v73
	s_waitcnt lgkmcnt(0)
	s_nop 1
	v_mfma_f32_32x32x16_bf16 v[48:63], v[104:107], v[108:111], v[48:63]
	v_mfma_f32_32x32x16_bf16 v[32:47], v[166:169], v[108:111], v[32:47]
	v_mfma_f32_32x32x16_bf16 v[16:31], v[170:173], v[108:111], v[16:31]
	v_mfma_f32_32x32x16_bf16 v[0:15], v[174:177], v[108:111], v[0:15]
	v_add_f32_e64 v96, v96, v98
	v_add_f32_e64 v97, v97, v99
	v_add_f32_e64 v92, v92, v94
	v_add_f32_e64 v93, v93, v95
	v_add_f32_e64 v88, v88, v90
	v_add_f32_e64 v89, v89, v91
	v_pk_add_f32 v[84:85], v[84:85], v[86:87]
	v_pk_add_f32 v[78:79], v[78:79], v[100:101]
	v_pk_add_f32 v[74:75], v[74:75], v[76:77]
	v_pk_add_f32 v[70:71], v[70:71], v[72:73]
	v_pk_add_f32 v[66:67], v[66:67], v[68:69]
	v_pk_add_f32 v[88:89], v[92:93], v[88:89]
	v_pk_add_f32 v[84:85], v[84:85], v[96:97]
	v_pk_add_f32 v[70:71], v[74:75], v[70:71]
	v_pk_add_f32 v[66:67], v[66:67], v[78:79]
	v_pk_add_f32 v[84:85], v[84:85], v[88:89]
	v_pk_add_f32 v[66:67], v[66:67], v[70:71]
	v_mov_b32_e32 v83, v64
	v_pk_add_f32 v[66:67], v[84:85], v[66:67]
	s_lshl_b32 s15, s8, 9
	v_pk_add_f32 v[66:67], v[66:67], v[66:67] op_sel_hi:[0,1]
	v_mov_b32_e32 v66, v193
	v_pk_add_f32 v[162:163], v[82:83], v[66:67]
	v_mad_i64_i32 v[66:67], s[8:9], v81, s21, 0
	v_pk_add_f32 v[64:65], v[162:163], 0 neg_lo:[1,1] neg_hi:[1,1]
	v_or_b32_e32 v66, v66, v80
	v_lshlrev_b32_e32 v65, 2, v102
	v_sub_u32_e32 v65, v192, v65
	v_lshl_add_u64 v[164:165], s[42:43], 0, v[66:67]
	v_mad_i64_i32 v[66:67], s[8:9], v103, s21, 0
	v_subrev_u32_e32 v65, s15, v65
	v_or_b32_e32 v66, v66, v80
	v_add_u32_e32 v222, s57, v65
	v_lshl_add_u64 v[166:167], s[42:43], 0, v[66:67]
	s_movk_i32 s60, 0xff00
	s_mov_b32 s73, 0x8000
	s_cmp_eq_u32 s40, 0
	s_cbranch_scc1 .Latt_prio_skip
	s_setprio 1
.Latt_prio_skip:
	v_lshl_add_u64 v[164:165], v[164:165], 0, s[50:51]
	v_lshl_add_u64 v[166:167], v[166:167], 0, s[50:51]
	v_add_co_u32_e32 v164, vcc, 0x392b1c00, v164
	s_nop 1
	v_addc_co_u32_e32 v165, vcc, 0, v165, vcc
	v_add_co_u32_e32 v166, vcc, 0x392b1c00, v166
	s_nop 1
	v_addc_co_u32_e32 v167, vcc, 0, v167, vcc
	v_mov_b32_e32 v65, v64
	v_mov_b32_e32 v66, v64
	v_mov_b32_e32 v67, v64
	v_mov_b32_e32 v68, v64
	v_mov_b32_e32 v69, v64
	v_mov_b32_e32 v70, v64
	v_mov_b32_e32 v71, v64
	v_mov_b32_e32 v72, v64
	v_mov_b32_e32 v73, v64
	v_mov_b32_e32 v74, v64
	v_mov_b32_e32 v75, v64
	v_mov_b32_e32 v76, v64
	v_mov_b32_e32 v77, v64
	v_mov_b32_e32 v78, v64
	v_mov_b32_e32 v79, v64
	s_barrier
	s_branch .LBB0_581

; #define LAS __attribute__((address_space(3)))
; __device__ __forceinline__ float swap_sum(float v) { float r0, r1; swap32(v, r0, r1); return r0 + r1; }
; __device__ __forceinline__ void attn_unit(const Frame& F, const bf16* __restrict__ proj, bf16* mix, const float* relb, const float* subg, int h, int qb, float lam, float one_m_li) {
;     ...
;     { const float lt = swap_sum(lsum); const float inv = 1.0f / lt;
; #pragma unroll
;       for (int eb = 0; eb < 4; ++eb)
; #pragma unroll
;           for (int r = 0; r < 16; ++r) o[eb][r] *= inv; }
;     LAS float* xch = (LAS float*)lds;
;     if (m == 1) {
; #pragma unroll
;         for (int eb = 0; eb < 4; ++eb)
; #pragma unroll
;             for (int r = 0; r < 16; ++r) xch[(wq * 64 + eb * 16 + r) * 64 + lane] = o[eb][r];
;     }
.LBB0_592:
	s_setprio 0
	v_mov_b32_e32 v64, v163
	s_nop 1
	v_permlane32_swap_b32 v163, v64
	s_nop 0
	v_add_f32_e32 v64, v163, v64
	v_div_scale_f32 v65, s[8:9], v64, v64, 1.0
	v_rcp_f32_e32 v66, v65
	v_div_scale_f32 v67, vcc, 1.0, v64, 1.0
	v_fma_f32 v68, -v65, v66, 1.0
	v_fmac_f32_e32 v66, v68, v66
	v_mul_f32_e32 v68, v67, v66
	v_fma_f32 v69, -v65, v68, v67
	v_fmac_f32_e32 v68, v69, v66
	v_fma_f32 v65, -v65, v68, v67
	v_div_fmas_f32 v65, v65, v66, v68
	v_div_fixup_f32 v76, v65, v64, 1.0
	v_pk_mul_f32 v[70:71], v[48:49], v[76:77] op_sel_hi:[1,0]
	v_pk_mul_f32 v[74:75], v[50:51], v[76:77] op_sel_hi:[1,0]
	v_pk_mul_f32 v[66:67], v[52:53], v[76:77] op_sel_hi:[1,0]
	v_pk_mul_f32 v[72:73], v[54:55], v[76:77] op_sel_hi:[1,0]
	v_pk_mul_f32 v[64:65], v[56:57], v[76:77] op_sel_hi:[1,0]
	v_pk_mul_f32 v[68:69], v[58:59], v[76:77] op_sel_hi:[1,0]
	v_pk_mul_f32 v[54:55], v[60:61], v[76:77] op_sel_hi:[1,0]
	v_pk_mul_f32 v[60:61], v[62:63], v[76:77] op_sel_hi:[1,0]
	v_pk_mul_f32 v[50:51], v[32:33], v[76:77] op_sel_hi:[1,0]
	v_pk_mul_f32 v[58:59], v[34:35], v[76:77] op_sel_hi:[1,0]
	v_pk_mul_f32 v[48:49], v[36:37], v[76:77] op_sel_hi:[1,0]
	v_pk_mul_f32 v[56:57], v[38:39], v[76:77] op_sel_hi:[1,0]
	v_pk_mul_f32 v[40:41], v[40:41], v[76:77] op_sel_hi:[1,0]
	v_pk_mul_f32 v[52:53], v[42:43], v[76:77] op_sel_hi:[1,0]
	v_pk_mul_f32 v[36:37], v[44:45], v[76:77] op_sel_hi:[1,0]
	v_pk_mul_f32 v[44:45], v[46:47], v[76:77] op_sel_hi:[1,0]
	v_pk_mul_f32 v[34:35], v[16:17], v[76:77] op_sel_hi:[1,0]
	v_pk_mul_f32 v[42:43], v[18:19], v[76:77] op_sel_hi:[1,0]
	v_pk_mul_f32 v[32:33], v[20:21], v[76:77] op_sel_hi:[1,0]
	v_pk_mul_f32 v[38:39], v[22:23], v[76:77] op_sel_hi:[1,0]
	v_pk_mul_f32 v[24:25], v[24:25], v[76:77] op_sel_hi:[1,0]
	v_pk_mul_f32 v[22:23], v[26:27], v[76:77] op_sel_hi:[1,0]
	v_pk_mul_f32 v[20:21], v[28:29], v[76:77] op_sel_hi:[1,0]
	v_pk_mul_f32 v[30:31], v[30:31], v[76:77] op_sel_hi:[1,0]
	v_pk_mul_f32 v[18:19], v[0:1], v[76:77] op_sel_hi:[1,0]
	v_pk_mul_f32 v[26:27], v[2:3], v[76:77] op_sel_hi:[1,0]
	v_pk_mul_f32 v[4:5], v[4:5], v[76:77] op_sel_hi:[1,0]
	v_pk_mul_f32 v[6:7], v[6:7], v[76:77] op_sel_hi:[1,0]
	v_pk_mul_f32 v[2:3], v[8:9], v[76:77] op_sel_hi:[1,0]
	v_pk_mul_f32 v[8:9], v[10:11], v[76:77] op_sel_hi:[1,0]
	v_pk_mul_f32 v[16:17], v[12:13], v[76:77] op_sel_hi:[1,0]
	v_pk_mul_f32 v[0:1], v[14:15], v[76:77] op_sel_hi:[1,0]
	s_and_b64 vcc, exec, s[6:7]
	s_cbranch_vccz .LBB0_594
	v_lshl_add_u32 v10, v213, 2, s53
	ds_write2st64_b32 v10, v70, v71 offset1:1
	ds_write2st64_b32 v10, v74, v75 offset0:2 offset1:3
	ds_write2st64_b32 v10, v66, v67 offset0:4 offset1:5
	ds_write2st64_b32 v10, v72, v73 offset0:6 offset1:7
	ds_write2st64_b32 v10, v64, v65 offset0:8 offset1:9
	ds_write2st64_b32 v10, v68, v69 offset0:10 offset1:11
	ds_write2st64_b32 v10, v54, v55 offset0:12 offset1:13
	ds_write2st64_b32 v10, v60, v61 offset0:14 offset1:15
	ds_write2st64_b32 v10, v50, v51 offset0:16 offset1:17
	ds_write2st64_b32 v10, v58, v59 offset0:18 offset1:19
	ds_write2st64_b32 v10, v48, v49 offset0:20 offset1:21
	ds_write2st64_b32 v10, v56, v57 offset0:22 offset1:23
	ds_write2st64_b32 v10, v40, v41 offset0:24 offset1:25
	ds_write2st64_b32 v10, v52, v53 offset0:26 offset1:27
	ds_write2st64_b32 v10, v36, v37 offset0:28 offset1:29
	ds_write2st64_b32 v10, v44, v45 offset0:30 offset1:31
	ds_write2st64_b32 v10, v34, v35 offset0:32 offset1:33
	ds_write2st64_b32 v10, v42, v43 offset0:34 offset1:35
	ds_write2st64_b32 v10, v32, v33 offset0:36 offset1:37
	ds_write2st64_b32 v10, v38, v39 offset0:38 offset1:39
	ds_write2st64_b32 v10, v24, v25 offset0:40 offset1:41
	ds_write2st64_b32 v10, v22, v23 offset0:42 offset1:43
	ds_write2st64_b32 v10, v20, v21 offset0:44 offset1:45
	ds_write2st64_b32 v10, v30, v31 offset0:46 offset1:47
	ds_write2st64_b32 v10, v18, v19 offset0:48 offset1:49
	ds_write2st64_b32 v10, v26, v27 offset0:50 offset1:51
	ds_write2st64_b32 v10, v4, v5 offset0:52 offset1:53
	ds_write2st64_b32 v10, v6, v7 offset0:54 offset1:55
	ds_write2st64_b32 v10, v2, v3 offset0:56 offset1:57
	ds_write2st64_b32 v10, v8, v9 offset0:58 offset1:59
	ds_write2st64_b32 v10, v16, v17 offset0:60 offset1:61
	ds_write2st64_b32 v10, v0, v1 offset0:62 offset1:63
